# warmkarg
# speedup vs baseline: 1.0355x; 1.0146x over previous
_Z11prep_kernelPKfS0_PKiS2_S0_S0_S0_S0_S0_S0_Pc:
	s_getpc_b64 s[36:37]
	s_add_u32 s36, s36, _Z11attn_kernelILi4EEvPKfS1_S1_S1_S1_S1_PKcPf@rel32@lo+4
	s_addc_u32 s37, s37, _Z11attn_kernelILi4EEvPKfS1_S1_S1_S1_S1_PKcPf@rel32@hi+12
	v_and_b32_e32 v192, 63, v0
	v_lshlrev_b32_e32 v192, 7, v192
	v_min_u32_e32 v192, 0x1180, v192
	global_load_dword v192, v192, s[36:37]
	s_lshr_b32 s4, s2, 2
	v_lshrrev_b32_e32 v2, 6, v0
	s_and_b32 s4, s4, 0x1ffffffe
	s_load_dwordx4 s[28:31], s[0:1], 0x40
	s_load_dwordx8 s[12:19], s[0:1], 0x0
	s_load_dwordx8 s[20:27], s[0:1], 0x20
	s_load_dwordx2 s[32:33], s[0:1], 0x50
	s_load_dword s40, s[0:1], 0x80
	s_load_dword s41, s[0:1], 0x100
	s_load_dword s42, s[0:1], 0x180
	v_and_b32_e32 v1, 15, v0
	s_and_b32 s3, s2, 7
	v_or_b32_e32 v2, s4, v2
	v_lshl_or_b32 v88, v2, 3, s3
	v_cmp_gt_u32_e64 s[10:11], 14, v1
	v_mul_lo_u32 v7, v88, 14
	v_and_b32_e32 v105, 63, v0
	v_cndmask_b32_e64 v6, 13, v1, s[10:11]
	v_add_u32_e32 v2, v7, v6
	v_mul_u32_u24_e32 v4, 12, v2
	v_lshlrev_b32_e32 v5, 2, v6
	v_cmp_gt_u32_e64 s[8:9], 48, v105
	v_cmp_gt_u32_e64 s[6:7], 14, v105
	v_lshlrev_b32_e32 v118, 1, v0
	v_lshrrev_b32_e32 v104, 4, v0
	v_cndmask_b32_e64 v8, 0, v105, s[8:9]
	v_cndmask_b32_e64 v9, 0, v105, s[6:7]
	v_mad_u32_u24 v8, v88, 48, v8
	v_add_lshl_u32 v9, v7, v9, 2
	v_lshlrev_b32_e32 v8, 2, v8
	s_lshl_b32 s2, s2, 3
	s_and_b32 s2, s2, 0x78
	v_and_b32_e32 v106, 30, v118
	v_or_b32_e32 v107, s2, v104
	v_cmp_gt_u32_e64 s[2:3], 23, v106
	v_or_b32_e32 v10, 1, v106
	v_cmp_gt_u32_e64 s[4:5], 23, v10
	v_lshlrev_b32_e32 v11, 7, v106
	v_lshlrev_b32_e32 v10, 7, v10
	v_cndmask_b32_e64 v11, 0, v11, s[2:3]
	v_cndmask_b32_e64 v10, 0, v10, s[4:5]
	v_or_b32_e32 v11, v11, v107
	v_or_b32_e32 v10, v10, v107
	v_lshlrev_b32_e32 v11, 2, v11
	v_lshlrev_b32_e32 v10, 2, v10
	v_lshlrev_b32_e32 v12, 2, v107
	v_lshlrev_b32_e32 v119, 5, v0
	v_lshlrev_b32_e32 v13, 2, v0
	v_and_b32_e32 v109, 12, v13
	v_and_b32_e32 v91, 0xf80, v119
	v_lshl_or_b32 v91, v109, 2, v91
	v_or_b32_e32 v92, 0x1000, v91
	v_lshlrev_b32_e32 v90, 9, v2
	v_and_b32_e32 v16, 48, v0
	v_or_b32_e32 v90, v90, v16
	v_or_b32_e32 v112, 0x80, v0
	v_or_b32_e32 v111, 0x180, v0
	v_or_b32_e32 v108, 0x280, v0
	v_mov_b32_e32 v87, 0
	v_bfe_u32 v110, v0, 4, 2
	s_movk_i32 s34, 0x60
	v_lshrrev_b32_e32 v136, 1, v0
	v_lshrrev_b32_e32 v18, 3, v0
	v_and_b32_e32 v18, 4, v18
	v_and_b32_e32 v19, 24, v0
	v_and_b32_e32 v20, 2, v136
	v_or3_b32 v18, v18, v19, v20
	v_and_or_b32 v136, v136, s34, v18
	v_mul_u32_u24_e32 v18, 0x110, v109
	v_lshl_add_u32 v136, v136, 1, v18
	v_add_u32_e32 v137, 0x1100, v136
	v_add_u32_e32 v138, 0x2200, v136
	v_lshlrev_b32_e32 v18, 9, v88
	v_and_b32_e32 v19, 0x100, v119
	v_lshlrev_b32_e32 v20, 4, v0
	v_and_b32_e32 v20, 48, v20
	v_or3_b32 v139, v18, v19, v20
	v_and_b32_e32 v19, 8, v118
	v_and_b32_e32 v20, 64, v118
	v_or3_b32 v139, v139, v19, v20
	v_lshlrev_b32_e32 v19, 2, v110
	v_and_b32_e32 v20, 4, v19
	v_or_b32_e32 v139, v139, v20
	v_lshl_or_b32 v140, v1, 5, v18
	v_or_b32_e32 v140, v140, v19
	v_add_u32_e32 v140, 0x80000, v140
	v_lshl_or_b32 v141, v88, 4, v1
	v_lshlrev_b32_e32 v141, 3, v141
	v_add_u32_e32 v141, 0x140000, v141
	v_lshlrev_b32_e32 v20, 8, v88
	v_mul_u32_u24_e32 v21, 43, v105
	v_lshrrev_b32_e32 v21, 9, v21
	v_mul_u32_u24_e32 v21, 12, v21
	v_sub_u32_e32 v22, v105, v21
	v_and_b32_e32 v142, 3, v22
	v_lshrrev_b32_e32 v22, 2, v22
	v_mad_u32_u24 v142, v142, 3, v22
	v_add_u32_e32 v142, v142, v21
	v_lshl_add_u32 v142, v142, 2, v20
	v_add_u32_e32 v142, 0x164000, v142
	v_lshl_add_u32 v143, v105, 2, v20
	v_add_u32_e32 v143, 0x164000, v143
	v_lshlrev_b32_e32 v123, 6, v107
	v_lshl_add_u32 v123, v106, 1, v123
	v_add_u32_e32 v123, 0x160000, v123
	v_lshl_add_u32 v122, v1, 4, v20
	v_or_b32_e32 v122, v122, v19
	v_add_u32_e32 v122, 0x100000, v122
	s_waitcnt lgkmcnt(0)
	global_load_dwordx3 v[82:84], v4, s[12:13]
	global_load_dword v85, v5, s[26:27]
	global_load_dword v114, v8, s[18:19]
	global_load_dword v115, v9, s[16:17]
	global_load_dword v116, v11, s[28:29]
	global_load_dword v113, v10, s[28:29]
	global_load_dword v117, v12, s[30:31]
	global_load_dwordx4 v[66:69], v91, s[20:21]
	global_load_dwordx4 v[70:73], v91, s[20:21] offset:64
	global_load_dwordx4 v[74:77], v92, s[20:21]
	global_load_dwordx4 v[78:81], v92, s[20:21] offset:64
	global_load_dwordx4 v[58:61], v91, s[22:23]
	global_load_dwordx4 v[62:65], v91, s[22:23] offset:64
	global_load_dwordx4 v[50:53], v92, s[22:23]
	global_load_dwordx4 v[54:57], v92, s[22:23] offset:64
	global_load_dwordx4 v[42:45], v91, s[24:25]
	global_load_dwordx4 v[46:49], v91, s[24:25] offset:64
	global_load_dwordx4 v[34:37], v92, s[24:25]
	global_load_dwordx4 v[38:41], v92, s[24:25] offset:64
	global_load_dwordx4 v[26:29], v90, s[14:15] nt
	global_load_dwordx4 v[30:33], v90, s[14:15] offset:64 nt
	global_load_dwordx4 v[18:21], v90, s[14:15] offset:128 nt
	global_load_dwordx4 v[22:25], v90, s[14:15] offset:192 nt
	global_load_dwordx4 v[10:13], v90, s[14:15] offset:256 nt
	global_load_dwordx4 v[14:17], v90, s[14:15] offset:320 nt
	global_load_dwordx4 v[2:5], v90, s[14:15] offset:384 nt
	global_load_dwordx4 v[6:9], v90, s[14:15] offset:448 nt
	s_waitcnt vmcnt(26)
	v_mov_b32_e32 v90, v83
	v_mov_b32_e32 v91, v84
	v_lshlrev_b32_e32 v86, 2, v110
	s_waitcnt vmcnt(25)
	v_mul_f32_e32 v84, 0x3fb8aa3b, v85
	s_mov_b32 s14, 0x41700000
	v_exp_f32_e32 v84, v84
	v_cndmask_b32_e64 v94, 0, 1.0, s[10:11]
	v_add_f32_e32 v84, 1.0, v84
	v_cmp_lt_f32_e32 vcc, s14, v85
	v_log_f32_e32 v84, v84
	v_cmp_lt_u32_e64 s[12:13], 15, v105
	v_mul_f32_e32 v84, 0x3f317218, v84
	v_cndmask_b32_e32 v84, v84, v85, vcc
	v_mul_f32_e32 v84, 0xbe715bef, v84
	v_mul_f32_e32 v84, 0x3f3504f3, v84
	v_mul_f32_e32 v84, 0x41800000, v84
	v_cndmask_b32_e64 v99, 0, v84, s[10:11]
	v_mul_f32_e32 v101, -2.0, v99
	v_mul_f32_e32 v100, v82, v82
	v_cmp_gt_u32_e32 vcc, 16, v105
	v_fmac_f32_e32 v100, v90, v90
	v_cmp_eq_u32_e64 s[12:13], 0, v110
	v_fmac_f32_e32 v100, v91, v91
	v_cmp_eq_u32_e64 s[14:15], 1, v110
	v_mul_f32_e32 v83, v101, v82
	v_cmp_eq_u32_e64 s[16:17], 2, v110
	v_mul_f32_e32 v84, v101, v90
	v_mul_f32_e32 v85, v101, v91
	v_mul_f32_e32 v89, v99, v100
	v_mul_f32_e32 v92, v82, v94
	v_mul_f32_e32 v93, v90, v94
	v_mul_f32_e32 v95, v91, v94
	v_mul_f32_e32 v96, v100, v94
	v_cvt_pk_fp8_f32 v88, v83, v83
	v_cvt_pk_fp8_f32 v104, v84, v84
	v_cvt_f32_fp8_e32 v97, v88
	v_cvt_f32_fp8_e32 v98, v104
	v_sub_f32_e32 v97, v83, v97
	v_sub_f32_e32 v98, v84, v98
	v_cvt_pk_fp8_f32 v88, v85, v85
	v_cvt_pk_fp8_f32 v104, v99, v99
	v_cvt_f32_fp8_e32 v101, v88
	v_cvt_f32_fp8_e32 v102, v104
	v_sub_f32_e32 v101, v85, v101
	v_sub_f32_e32 v102, v99, v102
	v_cvt_pk_fp8_f32 v88, v89, v89
	v_cvt_pk_fp8_f32 v104, v92, v92
	v_cvt_f32_fp8_e32 v103, v88
	v_cvt_f32_fp8_e32 v120, v104
	v_sub_f32_e32 v103, v89, v103
	v_sub_f32_e32 v120, v92, v120
	v_cvt_pk_fp8_f32 v88, v93, v93
	v_cvt_pk_fp8_f32 v104, v95, v95
	v_cvt_f32_fp8_e32 v121, v88
	v_cvt_f32_fp8_e32 v86, v104
	v_sub_f32_e32 v121, v93, v121
	v_sub_f32_e32 v86, v95, v86
	v_cvt_pk_fp8_f32 v88, v96, v96
	s_nop 0
	v_cvt_f32_fp8_e32 v87, v88
	s_nop 0
	v_sub_f32_e32 v87, v96, v87
	v_cndmask_b32_e64 v124, v89, v85, s[16:17]
	v_cndmask_b32_e64 v124, v124, v98, s[14:15]
	v_cndmask_b32_e64 v124, v124, v83, s[12:13]
	v_cndmask_b32_e64 v125, v103, v99, s[16:17]
	v_cndmask_b32_e64 v125, v125, v84, s[14:15]
	v_cndmask_b32_e64 v125, v125, v97, s[12:13]
	v_cndmask_b32_e64 v126, 0, v102, s[16:17]
	v_cndmask_b32_e64 v126, v126, v85, s[14:15]
	v_cndmask_b32_e64 v126, v126, v83, s[12:13]
	v_cndmask_b32_e64 v127, 0, v99, s[16:17]
	v_cndmask_b32_e64 v127, v127, v101, s[14:15]
	v_cndmask_b32_e64 v127, v127, v84, s[12:13]
	v_cndmask_b32_e64 v128, v94, v86, s[16:17]
	v_cndmask_b32_e64 v128, v128, v93, s[14:15]
	v_cndmask_b32_e64 v128, v128, v92, s[12:13]
	v_cndmask_b32_e64 v129, v94, v96, s[16:17]
	v_cndmask_b32_e64 v129, v129, v121, s[14:15]
	v_cndmask_b32_e64 v129, v129, v92, s[12:13]
	v_cndmask_b32_e64 v130, 0, v96, s[16:17]
	v_cndmask_b32_e64 v130, v130, v95, s[14:15]
	v_cndmask_b32_e64 v130, v130, v120, s[12:13]
	v_cndmask_b32_e64 v131, 0, v87, s[16:17]
	v_cndmask_b32_e64 v131, v131, v95, s[14:15]
	v_cndmask_b32_e64 v131, v131, v93, s[12:13]
	v_cvt_pk_fp8_f32 v119, v124, v125
	v_cvt_pk_fp8_f32 v103, v128, v129
	v_cvt_pk_fp8_f32 v119, v126, v127 op_sel:[0,0,1]
	v_cvt_pk_fp8_f32 v103, v130, v131 op_sel:[0,0,1]
	s_nop 0
	global_store_dword v139, v119, s[32:33] offset:128
	global_store_dword v140, v103, s[32:33] offset:16
	s_and_saveexec_b64 s[0:1], vcc
	s_cbranch_execz .LBB0_14
	v_cvt_f16_f32_e32 v83, v82
	v_cvt_pk_f16_f32 v90, v90, v91
	s_nop 0
	v_alignbit_b32 v91, 0, v90, 16
	v_pack_b32_f16 v90, v83, v90
	global_store_dwordx2 v141, v[90:91], s[32:33]
